# baseline (speedup 1.0000x reference)
.LBB2_2:
	s_or_b64 exec, exec, s[0:1]
	v_or_b32_e32 v55, v57, v55
	s_movk_i32 s0, 0x80
	v_cmp_gt_u32_e32 vcc, s0, v55
	v_or_b32_e32 v55, v75, v74
	s_movk_i32 s1, 0xb4
	s_waitcnt vmcnt(9)
	v_cndmask_b32_e32 v21, 0, v21, vcc
	v_cndmask_b32_e32 v20, 0, v20, vcc
	v_cndmask_b32_e32 v19, 0, v19, vcc
	v_cndmask_b32_e32 v18, 0, v18, vcc
	s_waitcnt vmcnt(8)
	v_cndmask_b32_e32 v25, 0, v25, vcc
	v_cndmask_b32_e32 v24, 0, v24, vcc
	v_cndmask_b32_e32 v23, 0, v23, vcc
	v_cndmask_b32_e32 v22, 0, v22, vcc
	v_cmp_gt_u32_e32 vcc, s0, v55
	v_or_b32_e32 v54, v56, v54
	v_lshrrev_b32_e32 v55, 2, v1
	s_waitcnt vmcnt(7)
	v_cndmask_b32_e32 v29, 0, v29, vcc
	v_cndmask_b32_e32 v28, 0, v28, vcc
	v_cndmask_b32_e32 v27, 0, v27, vcc
	v_cndmask_b32_e32 v26, 0, v26, vcc
	s_waitcnt vmcnt(6)
	v_cndmask_b32_e32 v33, 0, v33, vcc
	v_cndmask_b32_e32 v32, 0, v32, vcc
	v_cndmask_b32_e32 v31, 0, v31, vcc
	v_cndmask_b32_e32 v30, 0, v30, vcc
	v_cmp_gt_u32_e32 vcc, s1, v51
	v_cmp_gt_u32_e64 s[0:1], s0, v54
	s_and_b64 vcc, vcc, s[0:1]
	s_waitcnt vmcnt(5)
	v_cndmask_b32_e32 v37, 0, v37, vcc
	v_cndmask_b32_e32 v36, 0, v36, vcc
	v_cndmask_b32_e32 v35, 0, v35, vcc
	v_cndmask_b32_e32 v34, 0, v34, vcc
	s_waitcnt vmcnt(4)
	v_cndmask_b32_e32 v41, 0, v41, vcc
	v_cndmask_b32_e32 v40, 0, v40, vcc
	v_cndmask_b32_e32 v39, 0, v39, vcc
	v_cndmask_b32_e32 v38, 0, v38, vcc
	v_cmp_ne_u32_e32 vcc, 0, v42
	v_or_b32_e32 v75, v48, v55
	v_and_b32_e32 v56, 3, v0
	v_cndmask_b32_e64 v42, 0, 3, vcc
	v_add_u32_e32 v42, v42, v0
	v_and_b32_e32 v42, 15, v42
	v_mul_u32_u24_e32 v57, 0x3c00, v52
	v_mul_u32_u24_e32 v74, 0x2800, v52
	v_mul_u32_u24_e32 v75, 0x50, v75
	v_lshlrev_b32_e32 v76, 5, v45
	s_mov_b32 s5, s12
	s_movk_i32 s13, 0x50
	v_add3_u32 v74, v74, v75, v76
	v_lshlrev_b32_e32 v75, 3, v56
	v_or_b32_e32 v57, v57, v48
	v_mad_u32_u24 v48, v53, 18, v42
	s_lshl_b64 s[14:15], s[4:5], 14
	v_cmp_ne_u32_e64 s[4:5], 0, v56
	v_cmp_ne_u32_e64 s[6:7], 1, v56
	v_cmp_eq_u32_e64 s[8:9], 2, v56
	v_mul_u32_u24_e32 v56, 0x50, v49
	v_mov_b32_e32 v49, 0x5a0
	v_mad_u32_u24 v93, v48, s13, v49
	v_mov_b32_e32 v49, 0xa0
	v_mad_u32_u24 v92, v48, s13, v49
	v_mov_b32_e32 v49, 0x5f0
	v_mad_u32_u24 v94, v48, s13, v49
	v_mov_b32_e32 v49, 0x640
	v_mad_u32_u24 v95, v48, s13, v49
	v_mov_b32_e32 v49, 0xb40
	v_mad_u32_u24 v96, v48, s13, v49
	v_mov_b32_e32 v49, 0xb90
	s_movk_i32 s0, 0x7800
	s_movk_i32 s18, 0x2300
	v_lshlrev_b32_e32 v52, 12, v52
	v_mad_u32_u24 v97, v48, s13, v49
	v_mov_b32_e32 v49, 0xbe0
	v_lshl_or_b32 v54, v53, 4, v42
	v_add3_u32 v74, v74, v75, s0
	v_mov_b32_e32 v75, 0x7800
	v_lshlrev_b32_e32 v76, 8, v46
	v_mul_u32_u24_e32 v77, 0x50, v48
	v_mad_u32_u24 v91, v48, s13, s13
	v_mad_u32_u24 v98, v48, s13, v49
	v_mad_u32_u24 v48, v50, s18, v52
	v_lshlrev_b32_e32 v49, 10, v45
	v_mad_u32_u24 v54, v54, s13, v75
	v_mul_u32_u24_e32 v75, 0x2300, v50
	v_add3_u32 v48, v48, v49, v76
	v_lshlrev_b32_e32 v49, 2, v1
	v_lshlrev_b32_e32 v45, 6, v45
	v_cmp_eq_u32_e64 s[0:1], v55, v46
	v_and_b32_e32 v55, 0x100, v0
	v_or3_b32 v45, v75, v45, v49
	s_mov_b32 s13, 0xe900
	v_add3_u32 v84, v45, v55, s13
	v_add_u32_e32 v85, 0xe800, v45
	s_and_b32 s13, s2, 7
	v_lshlrev_b32_e32 v45, 7, v53
	v_lshl_or_b32 v45, s13, 11, v45
	v_lshl_or_b32 v45, s25, 10, v45
	v_or_b32_e32 v45, s14, v45
	v_or_b32_e32 v1, v48, v49
	v_mov_b32_e32 v49, s15
	v_or_b32_e32 v48, s26, v45
	v_lshl_add_u64 v[42:43], v[48:49], 0, v[42:43]
	v_lshlrev_b64 v[42:43], 7, v[42:43]
	s_mov_b32 s14, 0
	s_waitcnt lgkmcnt(0)
	v_and_or_b32 v42, v0, 48, v42
	s_mov_b32 s15, 0
	v_mul_u32_u24_e32 v47, 0x50, v47
	v_mul_u32_u24_e32 v51, 0x50, v51
	v_mul_u32_u24_e32 v100, 0x1400, v50
	v_lshl_add_u64 v[42:43], v[42:43], 0, s[14:15]
	v_add_u32_e32 v1, 0xc800, v1
	s_waitcnt lgkmcnt(0)
	v_lshl_add_u64 v[80:81], s[22:23], 0, v[42:43]
	v_lshl_add_u64 v[82:83], s[20:21], 0, v[42:43]
	v_mul_u32_u24_e32 v86, 0x90, v46
	s_mov_b64 s[18:19], 0
	v_add_u32_e32 v87, v57, v47
	v_add_u32_e32 v88, v57, v56
	v_add_u32_e32 v89, v57, v51
	v_add_u32_e32 v90, v77, v44
	v_add_u32_e32 v91, v91, v44
	v_add_u32_e32 v92, v92, v44
	v_add_u32_e32 v93, v93, v44
	v_add_u32_e32 v94, v94, v44
	v_add_u32_e32 v95, v95, v44
	v_add_u32_e32 v96, v96, v44
	v_add_u32_e32 v97, v97, v44
	v_add_u32_e32 v98, v98, v44
	v_add_u32_e32 v99, v54, v44
	v_add_u32_e32 v100, v74, v100
	v_add_u32_e32 v1, 0xfffff000, v1
	v_add_u32_e32 v84, 0xffffff00, v84
	v_add_u32_e32 v85, 0xffffff00, v85
	v_add_u32_e32 v86, 0x480, v86
	s_mov_b32 s25, 2
	global_load_dwordx4 v[2:5], v[4:5], off
	s_nop 0
	global_load_dwordx4 v[6:9], v[6:7], off
	s_nop 0
	global_load_dwordx4 v[10:13], v[12:13], off
	s_nop 0
	global_load_dwordx4 v[14:17], v[14:15], off
	s_branch .LBB2_7
